# P7/P8 next(): tstart/lcnt lane tables read once per phase into v252/v253; l/gsz division by exact multiply-shift instead of float reciprocal with two VALU round trips
# speedup vs baseline: 1.0159x; 1.0035x over previous
; #define PG8_STAGE(bufoff, gbase, voff) do { if constexpr (!(Sched::CRIP & 2)) _Pragma("unroll") for (int _i = 0; _i < 2; ++_i) { unsigned _o = (voff)[_i]; asm volatile("" : "+v"(_o)); \
;         __builtin_amdgcn_global_load_lds((const unsigned*)((const char*)(gbase) + _o), (LAS unsigned*)(lds + (bufoff) + ldsw + _i * 8192), 16, 0, 0); } } while (0)
; #define PG8_WAIT_V(n) asm volatile("s_waitcnt vmcnt(" #n ")" ::: "memory")
; #define PG8_BAR __builtin_amdgcn_s_barrier()
; template <class Epi, class Sched>
; __device__ __forceinline__ void gemm_phase(LAS unsigned char* lds, const Sched& S, const Epi& E) {
;     ...
;     PG8_STAGE(PG8_SB(0, 0), cB + PG8_KT(crot, 0), voffB); PG8_STAGE(PG8_SB(0, 1), cB + hstep + PG8_KT(crot, 0), voffB); PG8_STAGE(PG8_SA(0, 0), cA + PG8_KT(crot, 0), vA[0]); PG8_STAGE(PG8_SA(0, 1), cA + PG8_KT(crot, 0), vA[1]);
;     if (wr == 1) PG8_BAR;
;     PG8_WAIT_V(2); PG8_BAR;
;     PG8_STAGE(PG8_SB(1, 0), cB + PG8_KT(crot, 1), voffB); PG8_STAGE(PG8_SA(1, 0), cA + PG8_KT(crot, 1), vA[0]); PG8_STAGE(PG8_SB(1, 1), cB + hstep + PG8_KT(crot, 1), voffB);
;     PG8_WAIT_V(6); PG8_BAR;
;     ...
;                 int tz = threadIdx.x; asm volatile("" : "+v"(tz));
; #pragma unroll
;                 for (int i = 0; i < 2; ++i) { int R, C; stage_rc(tz * 16 + i * 8192, R, C);
; #pragma unroll
;                     for (int h = 0; h < 2; ++h) vA[h][i] = (unsigned)(lidx[h * HALF + R] * RP + C * 2); } } }
.LBB0_724:
	s_add_u32 s12, s88, 0x3a800000
	s_addc_u32 s13, s89, 0
	s_lshl_b32 s2, s2, 12
	s_addk_i32 s7, 0x80
	s_lshl_b32 s14, s3, 13
	s_and_b32 s15, s2, 0x3000
	s_and_b32 s7, s7, 0x780
	s_add_u32 s2, s28, s7
	v_mov_b32_e32 v2, v1
	s_waitcnt vmcnt(2)
	s_barrier
	s_addc_u32 s3, s29, 0
	s_add_i32 m0, s39, 0x18000
	v_lshlrev_b32_e32 v3, 6, v0
	global_load_lds_dwordx4 v2, s[2:3]
	v_mov_b32_e32 v2, v190
	s_add_i32 m0, s39, 0x1a000
	v_lshlrev_b32_e32 v5, 2, v0
	global_load_lds_dwordx4 v2, s[2:3]
	s_add_u32 s2, s58, s7
	s_addc_u32 s3, s59, 0
	v_mov_b32_e32 v2, v192
	s_add_i32 s70, s39, 0x8000
	s_mov_b32 m0, s70
	s_add_i32 s71, s39, 0xa000
	global_load_lds_dwordx4 v2, s[2:3]
	v_mov_b32_e32 v2, v194
	s_mov_b32 m0, s71
	v_and_b32_e32 v3, 0x3c0, v3
	global_load_lds_dwordx4 v2, s[2:3]
	s_add_u32 s2, s4, s7
	v_mov_b32_e32 v2, v1
	s_addc_u32 s3, s5, 0
	s_add_i32 m0, s39, 0x1c000
	v_and_b32_e32 v6, 32, v5
	global_load_lds_dwordx4 v2, s[2:3]
	v_mov_b32_e32 v2, v190
	s_add_i32 m0, s39, 0x1e000
	s_cmpk_lt_u32 s6, 0x100
	global_load_lds_dwordx4 v2, s[2:3]
	v_and_b32_e32 v2, 48, v0
	v_or_b32_e32 v4, v3, v2
	v_bitop3_b32 v2, v3, v6, v2 bitop3:0x36
	v_bitop3_b32 v3, s14, v4, v6 bitop3:0xf6
	v_or_b32_e32 v196, s15, v2
	s_cselect_b64 s[14:15], -1, 0
	s_add_i32 s3, 0, 0x27d04
	v_writelane_b32 v255, s3, 55
	s_add_i32 s3, 0, 0x27d4c
	v_writelane_b32 v255, s3, 56
	s_add_i32 s3, 0, 0x27d54
	v_writelane_b32 v255, s3, 57
	s_add_i32 s3, 0, 0x27d5c
	v_writelane_b32 v255, s3, 58
	s_add_i32 s3, 0, 0x27d64
	s_waitcnt vmcnt(0)
	v_writelane_b32 v255, s3, 59
	s_add_i32 s3, 0, 0x27d6c
	s_mov_b32 s4, 0
	s_add_i32 s2, 0, 0x27d80
	v_writelane_b32 v255, s3, 60
	s_add_i32 s3, 0, 0x27d74
	v_mov_b32_e32 v187, 0
	v_add_u32_e32 v197, s60, v5
	s_ashr_i32 s96, s96, 31
	s_add_i32 s9, 0, 0x27d0c
	s_add_i32 s8, 0, 0x27d14
	s_add_i32 s17, 0, 0x27d1c
	s_add_i32 s50, 0, 0x27d24
	s_add_i32 s10, 0, 0x27d2c
	s_add_i32 s11, 0, 0x27d34
	s_add_i32 s56, 0, 0x27d3c
	s_add_i32 s57, 0, 0x27d44
	v_writelane_b32 v255, s3, 61
	s_add_i32 s91, 0, 0x27d7c
	v_lshlrev_b32_e32 v198, 2, v0
	s_add_i32 s92, 0, 0x10000
	s_add_i32 s93, 0, 0x14000
	s_mov_b32 s5, s4
	s_mov_b32 s6, s4
	s_mov_b32 s7, s4
	s_mov_b32 s16, 0xc01d265f
	s_mov_b32 s94, 0xc15083aa
	s_mov_b32 s98, 0xbfd083aa
	v_mov_b32_e32 v199, s2
	v_add_u32_e32 v200, 0, v3
	v_mov_b32_e32 v201, 1
	v_mov_b32_e32 v42, 0xba1d265f
	v_mov_b32_e32 v46, 0xb9d083aa
	v_mov_b32_e32 v202, 0x411c62c0
	v_mov_b32_e32 v188, 0x3fd083aa
	s_mov_b32 s95, s4
	s_mov_b64 s[24:25], s[28:29]
	s_barrier
	v_mov_b32_e32 v4, v0
	s_nop 0
	v_ashrrev_i32_e32 v6, 31, v4
	v_lshrrev_b32_e32 v6, 26, v6
	v_lshlrev_b32_e32 v5, 4, v4
	v_add_u32_e32 v6, v4, v6
	v_bfe_i32 v4, v4, 27, 1
	v_lshrrev_b32_e32 v4, 22, v4
	v_add_u32_e32 v4, v5, v4
	v_and_b32_e32 v4, 0xfffffc00, v4
	v_sub_u32_e32 v4, v5, v4
	v_lshrrev_b32_e32 v7, 4, v4
	v_bitop3_b32 v4, v7, v4, 32 bitop3:0x6c
	v_ashrrev_i32_e32 v7, 31, v4
	v_lshrrev_b32_e32 v7, 26, v7
	v_ashrrev_i32_e32 v6, 6, v6
	v_add_u32_e32 v7, v4, v7
	v_ashrrev_i32_e32 v8, 6, v7
	v_lshlrev_b32_e32 v6, 5, v6
	v_and_b32_e32 v9, 32, v6
	v_and_b32_e32 v10, 0xc0, v7
	v_lshlrev_b32_e32 v7, 2, v8
	v_and_b32_e32 v6, 0xffffffc0, v6
	v_add3_u32 v6, s60, v7, v6
	v_mov_b32_e32 v246, v6
	v_sub_u32_e32 v4, v4, v10
	v_ashrrev_i16_sdwa v4, v201, sext(v4) dst_sel:DWORD dst_unused:UNUSED_PAD src0_sel:DWORD src1_sel:BYTE_0
	v_bfe_i32 v4, v4, 0, 16
	v_add_lshl_u32 v4, v9, v4, 1
	v_mov_b32_e32 v247, v4
	v_add_u32_e32 v4, 0x2000, v5
	v_ashrrev_i32_e32 v5, 31, v4
	v_lshrrev_b32_e32 v5, 22, v5
	v_add_u32_e32 v5, v4, v5
	v_ashrrev_i32_e32 v5, 10, v5
	v_mul_i32_i24_e32 v6, 0x400, v5
	v_sub_u32_e32 v4, v4, v6
	v_lshrrev_b32_e32 v6, 4, v4
	v_bitop3_b32 v4, v6, v4, 32 bitop3:0x6c
	v_ashrrev_i32_e32 v6, 31, v4
	v_lshrrev_b32_e32 v6, 26, v6
	v_add_u32_e32 v6, v4, v6
	v_ashrrev_i32_e32 v7, 6, v6
	v_lshlrev_b32_e32 v5, 5, v5
	v_and_b32_e32 v8, 32, v5
	v_and_b32_e32 v9, 0xc0, v6
	v_lshlrev_b32_e32 v6, 2, v7
	v_and_b32_e32 v5, 0xffffffc0, v5
	v_add3_u32 v5, s60, v6, v5
	v_mov_b32_e32 v248, v5
	v_sub_u32_e32 v4, v4, v9
	v_ashrrev_i16_sdwa v4, v201, sext(v4) dst_sel:DWORD dst_unused:UNUSED_PAD src0_sel:DWORD src1_sel:BYTE_0
	v_bfe_i32 v4, v4, 0, 16
	v_add_lshl_u32 v4, v8, v4, 1
	v_mov_b32_e32 v249, v4
	v_mbcnt_lo_u32_b32 v252, -1, 0
	v_mbcnt_hi_u32_b32 v252, -1, v252
	v_lshlrev_b32_e32 v252, 2, v252
	v_add_u32_e32 v253, 0x27e00, v252
	v_add_u32_e32 v252, 0x27d00, v252
	ds_read_b32 v253, v253
	ds_read_b32 v252, v252
	s_waitcnt lgkmcnt(0)
	s_branch .LBB0_727

; __device__ __forceinline__ bool tile_order(long L, int nM, int nN, int& pm, int& pn) {
;     const int nwg = nM * nN; if (L >= nwg) return false;
;     int wgid = (int)L; { const int q = nwg / 8, r = nwg % 8, xcd = wgid % 8, off = wgid / 8; wgid = (xcd < r ? xcd * (q + 1) : r * (q + 1) + (xcd - r) * q) + off; }
;     const int nig = WGM * nN, gid = wgid / nig, fm = gid * WGM, gsz = (nM - fm) < WGM ? (nM - fm) : WGM;
;     pm = fm + ((wgid % nig) % gsz); pn = (wgid % nig) / gsz; return true;
; }
;     __device__ __forceinline__ bool next(int i, Unit& u) const {
;         const int nM = __builtin_amdgcn_readfirstlane(tstart[NE]); int pm, pn; if (!tile_order((long)i * G + c, nM, nN, pm, pn)) return false;
;         int e = 0;
;         for (int j = 1; j < NE; ++j) e += (tstart[j] <= pm) ? 1 : 0;
;         e = __builtin_amdgcn_readfirstlane(e);
;         const int mt = __builtin_amdgcn_readfirstlane(pm - tstart[e]);
;         u.pm = pm; u.pn = pn; u.e = e;
;         u.avalid = __builtin_amdgcn_readfirstlane(cnt[e]) - mt * 256;
.LBB0_727:
	s_add_i32 s95, s95, 1
	s_mul_i32 s2, s95, s96
	s_mul_hi_u32 s3, s95, s33
	s_add_i32 s3, s3, s2
	s_mul_i32 s2, s95, s33
	v_readlane_b32 s18, v252, 32
	s_add_u32 s30, s2, s77
	s_addc_u32 s31, s3, s51
	s_lshl_b32 s2, s18, 4
	s_ashr_i32 s3, s2, 31
	v_mov_b64_e32 v[2:3], s[2:3]
	v_cmp_ge_i64_e32 vcc, s[30:31], v[2:3]
	v_cmp_lt_i64_e64 s[2:3], s[30:31], v[2:3]
	s_cbranch_vccnz .LBB0_729
	s_ashr_i32 s20, s30, 31
	s_lshr_b32 s20, s20, 29
	s_add_i32 s20, s30, s20
	s_ashr_i32 s21, s20, 3
	s_and_b32 s20, s20, -8
	s_sub_i32 s20, s30, s20
	v_mov_b32_e32 v2, s20
	v_alignbit_b32 v2, s18, v2, 31
	s_nop 0
	v_readfirstlane_b32 s22, v2
	s_mul_i32 s20, s20, s22
	s_add_i32 s20, s20, s21
	s_ashr_i32 s21, s20, 31
	s_lshr_b32 s21, s21, 26
	s_add_i32 s21, s20, s21
	s_ashr_i32 s22, s21, 6
	s_lshl_b32 s22, s22, 2
	s_sub_i32 s18, s18, s22
	s_min_i32 s18, s18, 4
	s_andn2_b32 s21, s21, 63
	s_sub_i32 s20, s20, s21
	s_sub_i32 s23, s18, 1
	s_lshl_b32 s23, s23, 3
	s_lshr_b32 s23, 0x3f557fff, s23
	s_and_b32 s23, s23, 0xff
	s_add_i32 s23, s23, 1
	s_mul_i32 s44, s20, s23
	s_lshr_b32 s44, s44, 8
	s_mul_i32 s18, s44, s18
	s_sub_i32 s18, s20, s18
	s_add_i32 s97, s22, s18
	v_cmp_ge_i32_e32 vcc, s97, v252
	s_nop 3
	s_and_b32 vcc_lo, vcc_lo, 0xfffffffe
	s_bcnt1_i32_b32 s20, vcc_lo
	s_nop 3
	v_readlane_b32 s18, v252, s20
	v_readlane_b32 s23, v253, s20
	s_ashr_i32 s21, s20, 31
	s_lshl_b64 s[24:25], s[20:21], 17
	s_sub_i32 s18, s97, s18
	s_lshl_b32 s22, s18, 8
	s_sub_i32 s90, s23, s22
	v_readlane_b32 s18, v255, 6
	s_add_u32 s18, s18, s24
	v_readlane_b32 s23, v255, 22
	s_addc_u32 s24, s23, s25
	s_ashr_i32 s23, s22, 31
	s_lshl_b64 s[22:23], s[22:23], 2
	s_add_u32 s22, s18, s22
	s_addc_u32 s23, s24, s23
	s_ashr_i32 s45, s44, 31
	s_lshl_b64 s[24:25], s[44:45], 19
	s_lshl_b64 s[30:31], s[20:21], 23
	v_readlane_b32 s18, v255, 51
	s_add_u32 s18, s18, s24
	v_readlane_b32 s21, v255, 52
	s_addc_u32 s21, s21, s25
	s_add_u32 s24, s18, s30
	s_addc_u32 s25, s21, s31

; #define PG8_STAGE(bufoff, gbase, voff) do { if constexpr (!(Sched::CRIP & 2)) _Pragma("unroll") for (int _i = 0; _i < 2; ++_i) { unsigned _o = (voff)[_i]; asm volatile("" : "+v"(_o)); \
;         __builtin_amdgcn_global_load_lds((const unsigned*)((const char*)(gbase) + _o), (LAS unsigned*)(lds + (bufoff) + ldsw + _i * 8192), 16, 0, 0); } } while (0)
; #define PG8_WAIT_V(n) asm volatile("s_waitcnt vmcnt(" #n ")" ::: "memory")
; #define PG8_BAR __builtin_amdgcn_s_barrier()
; template <class Epi, class Sched>
; __device__ __forceinline__ void gemm_phase(LAS unsigned char* lds, const Sched& S, const Epi& E) {
;     ...
;     PG8_STAGE(PG8_SB(0, 0), cB + PG8_KT(crot, 0), voffB); PG8_STAGE(PG8_SB(0, 1), cB + hstep + PG8_KT(crot, 0), voffB); PG8_STAGE(PG8_SA(0, 0), cA + PG8_KT(crot, 0), vA[0]); PG8_STAGE(PG8_SA(0, 1), cA + PG8_KT(crot, 0), vA[1]);
;     if (wr == 1) PG8_BAR;
;     PG8_WAIT_V(2); PG8_BAR;
;     PG8_STAGE(PG8_SB(1, 0), cB + PG8_KT(crot, 1), voffB); PG8_STAGE(PG8_SA(1, 0), cA + PG8_KT(crot, 1), vA[0]); PG8_STAGE(PG8_SB(1, 1), cB + hstep + PG8_KT(crot, 1), voffB);
;     PG8_WAIT_V(6); PG8_BAR;
.LBB0_801:
	s_add_u32 s6, s88, 0x1000000
	s_addc_u32 s7, s89, 0
	s_lshl_b32 s14, s8, 13
	s_lshl_b32 s8, s24, 7
	s_lshl_b32 s1, s1, 12
	s_addk_i32 s8, 0x80
	s_and_b32 s1, s1, 0x3000
	s_and_b32 s8, s8, 0x780
	s_add_u32 s12, s28, s8
	v_mov_b32_e32 v2, v1
	s_waitcnt vmcnt(2)
	s_barrier
	s_addc_u32 s13, s29, 0
	s_add_i32 m0, s69, 0x18000
	v_lshlrev_b32_e32 v3, 6, v0
	global_load_lds_dwordx4 v2, s[12:13]
	v_mov_b32_e32 v2, v180
	s_add_i32 m0, s69, 0x1a000
	v_and_b32_e32 v3, 0x3c0, v3
	global_load_lds_dwordx4 v2, s[12:13]
	s_add_u32 s12, s26, s8
	s_addc_u32 s13, s27, 0
	v_mov_b32_e32 v2, v181
	s_add_i32 s74, s69, 0x8000
	s_mov_b32 m0, s74
	s_add_i32 s75, s69, 0xa000
	global_load_lds_dwordx4 v2, s[12:13]
	v_mov_b32_e32 v2, v182
	s_mov_b32 m0, s75
	s_add_u32 s8, s9, s8
	global_load_lds_dwordx4 v2, s[12:13]
	v_mov_b32_e32 v2, v1
	s_addc_u32 s9, s10, 0
	s_add_i32 m0, s69, 0x1c000
	v_lshlrev_b32_e32 v5, 2, v0
	global_load_lds_dwordx4 v2, s[8:9]
	v_mov_b32_e32 v2, v180
	s_add_i32 m0, s69, 0x1e000
	v_and_b32_e32 v5, 32, v5
	global_load_lds_dwordx4 v2, s[8:9]
	v_and_b32_e32 v2, 48, v0
	v_or_b32_e32 v4, v3, v2
	s_waitcnt vmcnt(0)
	s_cmpk_lt_u32 s0, 0x100
	v_bitop3_b32 v2, v3, v5, v2 bitop3:0x36
	v_bitop3_b32 v3, s14, v4, v5 bitop3:0xf6
	s_cselect_b64 s[8:9], -1, 0
	s_add_i32 s0, 0, 0x27d80
	v_or_b32_e32 v186, s1, v2
	s_ashr_i32 s76, s96, 31
	v_mov_b32_e32 v187, s0
	s_add_i32 s77, 0, 0x10000
	s_add_i32 s78, 0, 0x14000
	v_add_u32_e32 v188, 0, v3
	v_mov_b32_e32 v179, 0
	s_mov_b32 s10, 0x3a800000
	s_mov_b32 s79, 0xc3e00000
	v_mov_b32_e32 v189, 0x43e00000
	s_mov_b64 s[94:95], s[28:29]
	s_mov_b64 s[92:93], s[26:27]
	v_readlane_b32 s38, v255, 28
	s_barrier
	v_mbcnt_lo_u32_b32 v252, -1, 0
	v_mbcnt_hi_u32_b32 v252, -1, v252
	v_lshlrev_b32_e32 v252, 2, v252
	v_add_u32_e32 v252, 0x27d00, v252
	ds_read_b32 v252, v252
	s_waitcnt lgkmcnt(0)
	s_branch .LBB0_804

; __device__ __forceinline__ bool tile_order(long L, int nM, int nN, int& pm, int& pn) {
;     const int nwg = nM * nN; if (L >= nwg) return false;
;     int wgid = (int)L; { const int q = nwg / 8, r = nwg % 8, xcd = wgid % 8, off = wgid / 8; wgid = (xcd < r ? xcd * (q + 1) : r * (q + 1) + (xcd - r) * q) + off; }
;     const int nig = WGM * nN, gid = wgid / nig, fm = gid * WGM, gsz = (nM - fm) < WGM ? (nM - fm) : WGM;
;     pm = fm + ((wgid % nig) % gsz); pn = (wgid % nig) / gsz; return true;
; }
;     __device__ __forceinline__ bool next(int i, Unit& u) const {
;         const int nM = __builtin_amdgcn_readfirstlane(tstart[NE]); int pm, pn; if (!tile_order((long)i * G + c, nM, nN, pm, pn)) return false;
;         int e = 0;
;         for (int j = 1; j < NE; ++j) e += (tstart[j] <= pm) ? 1 : 0;
;         e = __builtin_amdgcn_readfirstlane(e);
;         const int mt = __builtin_amdgcn_readfirstlane(pm - tstart[e]);
;         u.pm = pm; u.pn = pn; u.e = e;
.LBB0_804:
	s_add_i32 s73, s73, 1
	s_mul_i32 s0, s73, s76
	s_mul_hi_u32 s1, s73, s33
	s_add_i32 s1, s1, s0
	s_mul_i32 s0, s73, s33
	v_readlane_b32 s13, v252, 32
	s_add_u32 s30, s0, s38
	s_addc_u32 s31, s1, s48
	s_lshl_b32 s0, s13, 3
	s_ashr_i32 s1, s0, 31
	v_mov_b64_e32 v[2:3], s[0:1]
	v_cmp_ge_i64_e32 vcc, s[30:31], v[2:3]
	v_cmp_lt_i64_e64 s[0:1], s[30:31], v[2:3]
	s_cbranch_vccnz .LBB0_806
	s_ashr_i32 s12, s30, 31
	s_lshr_b32 s12, s12, 29
	s_add_i32 s12, s30, s12
	s_ashr_i32 s14, s12, 3
	s_and_b32 s12, s12, -8
	s_sub_i32 s12, s30, s12
	s_lshr_b32 s15, s12, 31
	s_add_i32 s15, s13, s15
	s_mul_i32 s12, s12, s15
	s_add_i32 s12, s12, s14
	s_ashr_i32 s14, s12, 31
	s_lshr_b32 s14, s14, 27
	s_add_i32 s14, s12, s14
	s_ashr_i32 s15, s14, 5
	s_lshl_b32 s15, s15, 2
	s_sub_i32 s13, s13, s15
	s_min_i32 s13, s13, 4
	s_andn2_b32 s14, s14, 31
	s_sub_i32 s14, s12, s14
	s_sub_i32 s16, s13, 1
	s_lshl_b32 s16, s16, 3
	s_lshr_b32 s16, 0x3f557fff, s16
	s_and_b32 s16, s16, 0xff
	s_add_i32 s16, s16, 1
	s_mul_i32 s12, s14, s16
	s_lshr_b32 s12, s12, 8
	s_mul_i32 s13, s12, s13
	s_sub_i32 s13, s14, s13
	s_add_i32 s14, s15, s13
	v_cmp_ge_i32_e32 vcc, s14, v252
	s_ashr_i32 s15, s14, 31
	s_lshl_b64 s[18:19], s[14:15], 19
	s_nop 3
	s_and_b32 vcc_lo, vcc_lo, 0xfffffffe
	s_bcnt1_i32_b32 s96, vcc_lo
	s_ashr_i32 s97, s96, 31
	s_add_u32 s92, s43, s18
	s_addc_u32 s93, s44, s19
	s_ashr_i32 s13, s12, 31
	s_lshl_b64 s[20:21], s[12:13], 19
	s_lshl_b64 s[30:31], s[96:97], 22
	s_add_u32 s13, s45, s20
	s_addc_u32 s15, s46, s21
	s_add_u32 s94, s13, s30
	s_addc_u32 s95, s15, s31
